# attention band mask: scalar branch on the boundary kind + pipelined compare/select pairs; scan: second workgroup barrier mid-step so only the first 36 fragments gate the step start
# speedup vs baseline: 1.0050x; 1.0036x over previous
.LBB0_668:
	s_andn2_b64 vcc, exec, s[0:1]
	s_cbranch_vccnz .LBB0_670
	v_lshl_add_u32 v130, s14, 6, v171
	s_cmp_eq_u32 s14, 0
	s_cbranch_scc0 .Lattn_mask_hi
	v_or_b32_e32 v181, 1, v130
	s_nop 0
	v_cmp_ge_i32_e32 vcc, v130, v172
	v_cmp_ge_i32_e64 s[0:1], v181, v172
	v_or_b32_e32 v180, 2, v130
	v_or_b32_e32 v181, 3, v130
	v_cndmask_b32_e32 v50, v240, v50, vcc
	v_cndmask_b32_e64 v51, v240, v51, s[0:1]
	v_cmp_ge_i32_e32 vcc, v180, v172
	v_cmp_ge_i32_e64 s[0:1], v181, v172
	v_or_b32_e32 v180, 8, v130
	v_or_b32_e32 v181, 9, v130
	v_cndmask_b32_e32 v52, v240, v52, vcc
	v_cndmask_b32_e64 v53, v240, v53, s[0:1]
	v_cmp_ge_i32_e32 vcc, v180, v172
	v_cmp_ge_i32_e64 s[0:1], v181, v172
	v_or_b32_e32 v180, 10, v130
	v_or_b32_e32 v181, 11, v130
	v_cndmask_b32_e32 v54, v240, v54, vcc
	v_cndmask_b32_e64 v55, v240, v55, s[0:1]
	v_cmp_ge_i32_e32 vcc, v180, v172
	v_cmp_ge_i32_e64 s[0:1], v181, v172
	v_or_b32_e32 v180, 16, v130
	v_or_b32_e32 v181, 17, v130
	v_cndmask_b32_e32 v56, v240, v56, vcc
	v_cndmask_b32_e64 v57, v240, v57, s[0:1]
	v_cmp_ge_i32_e32 vcc, v180, v172
	v_cmp_ge_i32_e64 s[0:1], v181, v172
	v_or_b32_e32 v180, 18, v130
	v_or_b32_e32 v181, 19, v130
	v_cndmask_b32_e32 v58, v240, v58, vcc
	v_cndmask_b32_e64 v59, v240, v59, s[0:1]
	v_cmp_ge_i32_e32 vcc, v180, v172
	v_cmp_ge_i32_e64 s[0:1], v181, v172
	v_or_b32_e32 v180, 24, v130
	v_or_b32_e32 v181, 25, v130
	v_cndmask_b32_e32 v60, v240, v60, vcc
	v_cndmask_b32_e64 v61, v240, v61, s[0:1]
	v_cmp_ge_i32_e32 vcc, v180, v172
	v_cmp_ge_i32_e64 s[0:1], v181, v172
	v_or_b32_e32 v180, 26, v130
	v_or_b32_e32 v181, 27, v130
	v_cndmask_b32_e32 v62, v240, v62, vcc
	v_cndmask_b32_e64 v63, v240, v63, s[0:1]
	v_cmp_ge_i32_e32 vcc, v180, v172
	v_cmp_ge_i32_e64 s[0:1], v181, v172
	v_or_b32_e32 v180, 32, v130
	v_or_b32_e32 v181, 33, v130
	v_cndmask_b32_e32 v64, v240, v64, vcc
	v_cndmask_b32_e64 v65, v240, v65, s[0:1]
	v_cmp_ge_i32_e32 vcc, v180, v172
	v_cmp_ge_i32_e64 s[0:1], v181, v172
	v_or_b32_e32 v180, 34, v130
	v_or_b32_e32 v181, 35, v130
	v_cndmask_b32_e32 v34, v240, v34, vcc
	v_cndmask_b32_e64 v35, v240, v35, s[0:1]
	v_cmp_ge_i32_e32 vcc, v180, v172
	v_cmp_ge_i32_e64 s[0:1], v181, v172
	v_or_b32_e32 v180, 40, v130
	v_or_b32_e32 v181, 41, v130
	v_cndmask_b32_e32 v36, v240, v36, vcc
	v_cndmask_b32_e64 v37, v240, v37, s[0:1]
	v_cmp_ge_i32_e32 vcc, v180, v172
	v_cmp_ge_i32_e64 s[0:1], v181, v172
	v_or_b32_e32 v180, 42, v130
	v_or_b32_e32 v181, 43, v130
	v_cndmask_b32_e32 v38, v240, v38, vcc
	v_cndmask_b32_e64 v39, v240, v39, s[0:1]
	v_cmp_ge_i32_e32 vcc, v180, v172
	v_cmp_ge_i32_e64 s[0:1], v181, v172
	v_or_b32_e32 v180, 48, v130
	v_or_b32_e32 v181, 49, v130
	v_cndmask_b32_e32 v40, v240, v40, vcc
	v_cndmask_b32_e64 v41, v240, v41, s[0:1]
	v_cmp_ge_i32_e32 vcc, v180, v172
	v_cmp_ge_i32_e64 s[0:1], v181, v172
	v_or_b32_e32 v180, 50, v130
	v_or_b32_e32 v181, 51, v130
	v_cndmask_b32_e32 v42, v240, v42, vcc
	v_cndmask_b32_e64 v43, v240, v43, s[0:1]
	v_cmp_ge_i32_e32 vcc, v180, v172
	v_cmp_ge_i32_e64 s[0:1], v181, v172
	v_or_b32_e32 v180, 56, v130
	v_or_b32_e32 v181, 57, v130
	v_cndmask_b32_e32 v44, v240, v44, vcc
	v_cndmask_b32_e64 v45, v240, v45, s[0:1]
	v_cmp_ge_i32_e32 vcc, v180, v172
	v_cmp_ge_i32_e64 s[0:1], v181, v172
	v_or_b32_e32 v180, 58, v130
	v_or_b32_e32 v181, 59, v130
	v_cndmask_b32_e32 v46, v240, v46, vcc
	v_cndmask_b32_e64 v47, v240, v47, s[0:1]
	v_cmp_ge_i32_e32 vcc, v180, v172
	v_cmp_ge_i32_e64 s[0:1], v181, v172
	s_nop 1
	v_cndmask_b32_e32 v48, v240, v48, vcc
	v_cndmask_b32_e64 v49, v240, v49, s[0:1]
	s_branch .LBB0_670
.Lattn_mask_hi:
	v_or_b32_e32 v181, 1, v130
	s_nop 0
	v_cmp_le_i32_e32 vcc, v130, v173
	v_cmp_le_i32_e64 s[0:1], v181, v173
	v_or_b32_e32 v180, 2, v130
	v_or_b32_e32 v181, 3, v130
	v_cndmask_b32_e32 v50, v240, v50, vcc
	v_cndmask_b32_e64 v51, v240, v51, s[0:1]
	v_cmp_le_i32_e32 vcc, v180, v173
	v_cmp_le_i32_e64 s[0:1], v181, v173
	v_or_b32_e32 v180, 8, v130
	v_or_b32_e32 v181, 9, v130
	v_cndmask_b32_e32 v52, v240, v52, vcc
	v_cndmask_b32_e64 v53, v240, v53, s[0:1]
	v_cmp_le_i32_e32 vcc, v180, v173
	v_cmp_le_i32_e64 s[0:1], v181, v173
	v_or_b32_e32 v180, 10, v130
	v_or_b32_e32 v181, 11, v130
	v_cndmask_b32_e32 v54, v240, v54, vcc
	v_cndmask_b32_e64 v55, v240, v55, s[0:1]
	v_cmp_le_i32_e32 vcc, v180, v173
	v_cmp_le_i32_e64 s[0:1], v181, v173
	v_or_b32_e32 v180, 16, v130
	v_or_b32_e32 v181, 17, v130
	v_cndmask_b32_e32 v56, v240, v56, vcc
	v_cndmask_b32_e64 v57, v240, v57, s[0:1]
	v_cmp_le_i32_e32 vcc, v180, v173
	v_cmp_le_i32_e64 s[0:1], v181, v173
	v_or_b32_e32 v180, 18, v130
	v_or_b32_e32 v181, 19, v130
	v_cndmask_b32_e32 v58, v240, v58, vcc
	v_cndmask_b32_e64 v59, v240, v59, s[0:1]
	v_cmp_le_i32_e32 vcc, v180, v173
	v_cmp_le_i32_e64 s[0:1], v181, v173
	v_or_b32_e32 v180, 24, v130
	v_or_b32_e32 v181, 25, v130
	v_cndmask_b32_e32 v60, v240, v60, vcc
	v_cndmask_b32_e64 v61, v240, v61, s[0:1]
	v_cmp_le_i32_e32 vcc, v180, v173
	v_cmp_le_i32_e64 s[0:1], v181, v173
	v_or_b32_e32 v180, 26, v130
	v_or_b32_e32 v181, 27, v130
	v_cndmask_b32_e32 v62, v240, v62, vcc
	v_cndmask_b32_e64 v63, v240, v63, s[0:1]
	v_cmp_le_i32_e32 vcc, v180, v173
	v_cmp_le_i32_e64 s[0:1], v181, v173
	v_or_b32_e32 v180, 32, v130
	v_or_b32_e32 v181, 33, v130
	v_cndmask_b32_e32 v64, v240, v64, vcc
	v_cndmask_b32_e64 v65, v240, v65, s[0:1]
	v_cmp_le_i32_e32 vcc, v180, v173
	v_cmp_le_i32_e64 s[0:1], v181, v173
	v_or_b32_e32 v180, 34, v130
	v_or_b32_e32 v181, 35, v130
	v_cndmask_b32_e32 v34, v240, v34, vcc
	v_cndmask_b32_e64 v35, v240, v35, s[0:1]
	v_cmp_le_i32_e32 vcc, v180, v173
	v_cmp_le_i32_e64 s[0:1], v181, v173
	v_or_b32_e32 v180, 40, v130
	v_or_b32_e32 v181, 41, v130
	v_cndmask_b32_e32 v36, v240, v36, vcc
	v_cndmask_b32_e64 v37, v240, v37, s[0:1]
	v_cmp_le_i32_e32 vcc, v180, v173
	v_cmp_le_i32_e64 s[0:1], v181, v173
	v_or_b32_e32 v180, 42, v130
	v_or_b32_e32 v181, 43, v130
	v_cndmask_b32_e32 v38, v240, v38, vcc
	v_cndmask_b32_e64 v39, v240, v39, s[0:1]
	v_cmp_le_i32_e32 vcc, v180, v173
	v_cmp_le_i32_e64 s[0:1], v181, v173
	v_or_b32_e32 v180, 48, v130
	v_or_b32_e32 v181, 49, v130
	v_cndmask_b32_e32 v40, v240, v40, vcc
	v_cndmask_b32_e64 v41, v240, v41, s[0:1]
	v_cmp_le_i32_e32 vcc, v180, v173
	v_cmp_le_i32_e64 s[0:1], v181, v173
	v_or_b32_e32 v180, 50, v130
	v_or_b32_e32 v181, 51, v130
	v_cndmask_b32_e32 v42, v240, v42, vcc
	v_cndmask_b32_e64 v43, v240, v43, s[0:1]
	v_cmp_le_i32_e32 vcc, v180, v173
	v_cmp_le_i32_e64 s[0:1], v181, v173
	v_or_b32_e32 v180, 56, v130
	v_or_b32_e32 v181, 57, v130
	v_cndmask_b32_e32 v44, v240, v44, vcc
	v_cndmask_b32_e64 v45, v240, v45, s[0:1]
	v_cmp_le_i32_e32 vcc, v180, v173
	v_cmp_le_i32_e64 s[0:1], v181, v173
	v_or_b32_e32 v180, 58, v130
	v_or_b32_e32 v181, 59, v130
	v_cndmask_b32_e32 v46, v240, v46, vcc
	v_cndmask_b32_e64 v47, v240, v47, s[0:1]
	v_cmp_le_i32_e32 vcc, v180, v173
	v_cmp_le_i32_e64 s[0:1], v181, v173
	s_nop 1
	v_cndmask_b32_e32 v48, v240, v48, vcc
	v_cndmask_b32_e64 v49, v240, v49, s[0:1]

.LBB0_713:
	v_lshl_add_u64 v[68:69], s[6:7], 0, v[130:131]
	v_readlane_b32 s6, v252, 44
	v_readlane_b32 s7, v252, 45
	s_lshl_b32 s48, s36, 10
	s_add_i32 m0, s48, 0
	s_and_b32 s12, s14, 1
	global_load_lds_dwordx4 v[68:69], off
	s_nop 0
	global_load_dword v134, v131, s[6:7]
	s_or_b32 s74, s12, s44
	s_cmp_lt_i32 s14, 2
	s_cselect_b64 s[6:7], -1, 0
	s_sub_i32 s52, s16, 51
	s_lshr_b32 s52, s52, 3
	s_add_i32 s52, s52, s44
	s_sub_i32 s12, s16, 56
	s_lshl_b32 s68, s52, 11
	s_sub_i32 s52, s16, 50
	s_lshr_b32 s12, s12, 3
	s_lshr_b32 s52, s52, 3
	s_add_i32 s12, s12, s44
	s_add_i32 s52, s52, s44
	s_lshl_b32 s49, s14, 13
	s_lshl_b32 s40, s12, 11
	s_sub_i32 s12, s16, 55
	s_sub_i32 s14, s16, 54
	s_sub_i32 s42, s16, 53
	s_sub_i32 s46, s16, 52
	s_lshl_b32 s70, s52, 11
	s_sub_i32 s52, s16, 49
	s_lshr_b32 s12, s12, 3
	s_lshr_b32 s14, s14, 3
	s_lshr_b32 s42, s42, 3
	s_lshr_b32 s46, s46, 3
	s_lshr_b32 s52, s52, 3
	s_mov_b32 s41, s79
	s_add_i32 s12, s12, s44
	s_add_i32 s14, s14, s44
	s_add_i32 s42, s42, s44
	s_add_i32 s46, s46, s44
	s_add_i32 s52, s52, s44
	s_ashr_i32 s50, s16, 31
	s_lshl_b32 s12, s12, 11
	s_ashr_i32 s51, s18, 31
	s_lshl_b32 s14, s14, 11
	s_ashr_i32 s53, s20, 31
	s_lshl_b32 s42, s42, 11
	s_ashr_i32 s54, s22, 31
	s_lshl_b32 s46, s46, 11
	s_ashr_i32 s55, s24, 31
	s_ashr_i32 s56, s26, 31
	s_ashr_i32 s57, s28, 31
	s_lshl_b32 s72, s52, 11
	s_ashr_i32 s58, s30, 31
	s_lshl_b64 s[60:61], s[40:41], 2
	v_readlane_b32 s44, v252, 38
	s_add_u32 s52, s44, s60
	v_readlane_b32 s45, v252, 40
	s_addc_u32 s60, s45, s61
	s_lshl_b64 s[10:11], s[10:11], 2
	s_mov_b32 s13, s79
	s_add_u32 s59, s52, s10
	s_addc_u32 s60, s60, s11
	s_lshl_b64 s[12:13], s[12:13], 2
	s_add_u32 s12, s44, s12
	s_addc_u32 s13, s45, s13
	s_and_b32 s52, s19, 0x1c00
	s_mov_b32 s15, s79
	s_add_u32 s61, s12, s52
	s_addc_u32 s62, s13, 0
	s_lshl_b64 s[12:13], s[14:15], 2
	s_add_u32 s12, s44, s12
	s_addc_u32 s13, s45, s13
	s_and_b32 s14, s21, 0x1c00
	s_mov_b32 s43, s79
	s_add_u32 s63, s12, s14
	s_addc_u32 s64, s13, 0
	s_lshl_b64 s[12:13], s[42:43], 2
	s_add_u32 s12, s44, s12
	s_addc_u32 s13, s45, s13
	s_and_b32 s14, s23, 0x1c00
	s_mov_b32 s47, s79
	s_add_u32 s65, s12, s14
	s_addc_u32 s66, s13, 0
	s_lshl_b64 s[12:13], s[46:47], 2
	s_add_u32 s12, s44, s12
	s_addc_u32 s13, s45, s13
	s_and_b32 s14, s25, 0x1c00
	s_mov_b32 s69, s79
	s_add_u32 s67, s12, s14
	s_addc_u32 s86, s13, 0
	s_lshl_b64 s[12:13], s[68:69], 2
	s_add_u32 s12, s44, s12
	s_addc_u32 s13, s45, s13
	s_and_b32 s14, s27, 0x1c00
	s_mov_b32 s71, s79
	s_add_u32 s87, s12, s14
	s_addc_u32 s94, s13, 0
	s_lshl_b64 s[12:13], s[70:71], 2
	s_add_u32 s12, s44, s12
	s_addc_u32 s13, s45, s13
	s_and_b32 s14, s29, 0x1c00
	s_mov_b32 s73, s79
	s_add_u32 s95, s12, s14
	s_addc_u32 s96, s13, 0
	s_lshl_b64 s[12:13], s[72:73], 2
	s_add_u32 s12, s44, s12
	s_addc_u32 s13, s45, s13
	s_and_b32 s14, s31, 0x1c00
	s_add_u32 s97, s12, s14
	s_addc_u32 s42, s13, 0
	s_lshl_b64 s[8:9], s[8:9], 2
	s_add_u32 s8, s44, s8
	s_addc_u32 s9, s45, s9
	s_add_u32 s43, s8, s10
	s_addc_u32 s52, s9, s11
	s_lshl_b32 s8, s74, 6
	v_readlane_b32 s9, v252, 52
	v_and_b32_e32 v66, 31, v66
	s_add_u32 s8, s9, s8
	v_readlane_b32 s9, v252, 55
	v_lshrrev_b32_e32 v135, 5, v67
	v_readlane_b32 s40, v252, 16
	s_addc_u32 s9, s9, 0
	v_lshlrev_b32_e32 v66, 1, v66
	v_mov_b32_e32 v67, v131
	v_readlane_b32 s72, v252, 50
	v_mov_b32_e32 v3, v2
	v_mov_b32_e32 v4, v2
	v_mov_b32_e32 v5, v2
	v_mov_b32_e32 v6, v2
	v_mov_b32_e32 v7, v2
	v_mov_b32_e32 v8, v2
	v_mov_b32_e32 v9, v2
	v_mov_b32_e32 v10, v2
	v_mov_b32_e32 v11, v2
	v_mov_b32_e32 v12, v2
	v_mov_b32_e32 v13, v2
	v_mov_b32_e32 v14, v2
	v_mov_b32_e32 v15, v2
	v_mov_b32_e32 v16, v2
	v_mov_b32_e32 v17, v2
	v_mov_b32_e32 v19, v18
	v_mov_b32_e32 v20, v18
	v_mov_b32_e32 v21, v18
	v_mov_b32_e32 v22, v18
	v_mov_b32_e32 v23, v18
	v_mov_b32_e32 v24, v18
	v_mov_b32_e32 v25, v18
	v_mov_b32_e32 v26, v18
	v_mov_b32_e32 v27, v18
	v_mov_b32_e32 v28, v18
	v_mov_b32_e32 v29, v18
	v_mov_b32_e32 v30, v18
	v_mov_b32_e32 v31, v18
	v_mov_b32_e32 v32, v18
	v_mov_b32_e32 v33, v18
	v_mov_b32_e32 v35, v34
	v_mov_b32_e32 v36, v34
	v_mov_b32_e32 v37, v34
	v_mov_b32_e32 v38, v34
	v_mov_b32_e32 v39, v34
	v_mov_b32_e32 v40, v34
	v_mov_b32_e32 v41, v34
	v_mov_b32_e32 v42, v34
	v_mov_b32_e32 v43, v34
	v_mov_b32_e32 v44, v34
	v_mov_b32_e32 v45, v34
	v_mov_b32_e32 v46, v34
	v_mov_b32_e32 v47, v34
	v_mov_b32_e32 v48, v34
	v_mov_b32_e32 v49, v34
	v_mov_b32_e32 v51, v50
	v_mov_b32_e32 v52, v50
	v_mov_b32_e32 v53, v50
	v_mov_b32_e32 v54, v50
	v_mov_b32_e32 v55, v50
	v_mov_b32_e32 v56, v50
	v_mov_b32_e32 v57, v50
	v_mov_b32_e32 v58, v50
	v_mov_b32_e32 v59, v50
	v_mov_b32_e32 v60, v50
	v_mov_b32_e32 v61, v50
	v_mov_b32_e32 v62, v50
	v_mov_b32_e32 v63, v50
	v_mov_b32_e32 v64, v50
	v_mov_b32_e32 v65, v50
	v_add_u32_e32 v136, 0, v130
	v_readlane_b32 s41, v252, 17
	v_lshl_add_u64 v[132:133], s[8:9], 0, v[66:67]
	s_mov_b32 s46, 34
	s_mov_b32 s47, -4
	s_waitcnt vmcnt(0)
	v_mov_b32_e32 v137, v134
	v_readlane_b32 s44, v252, 37
	v_readlane_b32 s73, v252, 51
	v_readlane_b32 s45, v252, 46
	v_readlane_b32 s71, v252, 47
	v_readlane_b32 s74, v252, 48
	s_lshl_b32 s10, s16, 10
	s_add_u32 s10, s40, s10
	s_addc_u32 s11, s41, 0
	s_cmp_lg_u64 s[0:1], 0
	s_cselect_b32 s59, s59, s10
	s_cselect_b32 s60, s60, s11
	s_lshl_b32 s10, s18, 10
	s_add_u32 s10, s40, s10
	s_addc_u32 s11, s41, 0
	s_cmp_lg_u64 s[0:1], 0
	s_cselect_b32 s61, s61, s10
	s_cselect_b32 s62, s62, s11
	s_lshl_b32 s10, s20, 10
	s_add_u32 s10, s40, s10
	s_addc_u32 s11, s41, 0
	s_cmp_eq_u64 s[4:5], 0
	s_cselect_b32 s63, s63, s10
	s_cselect_b32 s64, s64, s11
	s_lshl_b32 s10, s22, 10
	s_add_u32 s10, s40, s10
	s_addc_u32 s11, s41, 0
	s_cmp_eq_u64 s[4:5], 0
	s_cselect_b32 s65, s65, s10
	s_cselect_b32 s66, s66, s11
	s_lshl_b32 s10, s24, 10
	s_add_u32 s10, s40, s10
	s_addc_u32 s11, s41, 0
	s_cmp_eq_u64 s[4:5], 0
	s_cselect_b32 s67, s67, s10
	s_cselect_b32 s86, s86, s11
	s_lshl_b32 s10, s26, 10
	s_add_u32 s10, s40, s10
	s_addc_u32 s11, s41, 0
	s_cmp_eq_u64 s[4:5], 0
	s_cselect_b32 s87, s87, s10
	s_cselect_b32 s94, s94, s11
	s_lshl_b32 s10, s28, 10
	s_add_u32 s10, s40, s10
	s_addc_u32 s11, s41, 0
	s_cmp_eq_u64 s[4:5], 0
	s_cselect_b32 s95, s95, s10
	s_cselect_b32 s96, s96, s11
	s_lshl_b32 s10, s30, 10
	s_add_u32 s10, s40, s10
	s_addc_u32 s11, s41, 0
	s_cmp_eq_u64 s[4:5], 0
	s_cselect_b32 s97, s97, s10
	s_cselect_b32 s42, s42, s11
	s_lshl_b32 s10, s36, 10
	s_add_u32 s10, s40, s10
	s_addc_u32 s11, s41, 0
	s_cmp_eq_u64 s[4:5], 0
	s_cselect_b32 s43, s43, s10
	s_cselect_b32 s52, s52, s11
	v_readfirstlane_b32 s2, v0
	s_nop 0
	s_lshr_b32 s2, s2, 8
	s_cmp_lg_u32 s2, 0
	s_cselect_b64 s[2:3], -1, 0
	s_branch .LBB0_716

.Lscan_w2:
	s_and_b64 vcc, exec, s[2:3]
	s_cbranch_vccz .Lscan_w23
	s_waitcnt vmcnt(10)
	s_barrier
	s_add_i32 s46, s46, -1
	s_add_i32 s47, s47, 1
	s_branch .LBB0_716
.Lscan_w23:
	s_barrier
	s_branch .LBB0_715
.Lscan_w2_last:
	s_waitcnt vmcnt(0)
	s_barrier
	s_branch .LBB0_715

.LBB0_716:
	s_add_i32 s68, s47, 4
	s_and_b64 vcc, exec, s[2:3]
	s_cbranch_vccnz .Lscan_top
	s_waitcnt vmcnt(0)

.LBB0_769:
	s_bitcmp1_b32 s68, 0
	s_cselect_b32 s8, 0x12000, 0
	v_add_u32_e32 v190, s8, v136
	v_mov_b32 v82, 0
	v_mov_b32 v66, 0
	ds_read_b128 v[98:101], v190
	ds_read_b128 v[138:141], v190 offset:1024
	ds_read_b128 v[102:105], v190 offset:16384
	ds_read_b128 v[142:145], v190 offset:17408
	ds_read_b128 v[146:149], v190 offset:8192
	ds_read_b128 v[150:153], v190 offset:9216
	ds_read_b128 v[154:157], v190 offset:24576
	ds_read_b128 v[158:161], v190 offset:25600
	v_mov_b32_e32 v83, v82
	v_mov_b32_e32 v84, v82
	v_mov_b32_e32 v85, v82
	v_mov_b32_e32 v86, v82
	v_mov_b32_e32 v87, v82
	v_mov_b32_e32 v88, v82
	v_mov_b32_e32 v89, v82
	v_mov_b32_e32 v90, v82
	v_mov_b32_e32 v91, v82
	v_mov_b32_e32 v92, v82
	v_mov_b32_e32 v93, v82
	v_mov_b32_e32 v94, v82
	v_mov_b32_e32 v95, v82
	v_mov_b32_e32 v96, v82
	v_mov_b32_e32 v97, v82
	v_mov_b32_e32 v67, v66
	v_mov_b32_e32 v68, v66
	v_mov_b32_e32 v69, v66
	v_mov_b32_e32 v70, v66
	v_mov_b32_e32 v71, v66
	v_mov_b32_e32 v72, v66
	v_mov_b32_e32 v73, v66
	v_mov_b32_e32 v74, v66
	v_mov_b32_e32 v75, v66
	v_mov_b32_e32 v76, v66
	v_mov_b32_e32 v77, v66
	v_mov_b32_e32 v78, v66
	v_mov_b32_e32 v79, v66
	v_mov_b32_e32 v80, v66
	v_mov_b32_e32 v81, v66
	v_add_u32_e32 v191, s49, v190
	ds_read_b128 v[162:165], v190 offset:2048
	ds_read_b128 v[166:169], v190 offset:3072
	ds_read_b128 v[170:173], v190 offset:18432
	ds_read_b128 v[174:177], v190 offset:19456
	ds_read_b128 v[178:181], v190 offset:10240
	ds_read_b128 v[182:185], v190 offset:11264
	ds_read_b128 v[186:189], v190 offset:26624
	ds_read_b128 v[198:201], v190 offset:27648
	v_cvt_pk_bf16_f32 v202, v2, v3
	v_cvt_pk_bf16_f32 v203, v4, v5
	v_cvt_pk_bf16_f32 v204, v6, v7
	v_cvt_pk_bf16_f32 v205, v8, v9
	s_waitcnt lgkmcnt(8)
	s_nop 0
	v_mfma_f32_32x32x16_bf16 v[114:129], v[98:101], v[202:205], v[82:97]
	v_mfma_f32_32x32x16_bf16 v[82:97], v[102:105], v[202:205], v[82:97]
	v_mfma_f32_32x32x16_bf16 v[98:113], v[146:149], v[202:205], v[66:81]
	v_cvt_pk_bf16_f32 v146, v10, v11
	v_cvt_pk_bf16_f32 v147, v12, v13
	v_cvt_pk_bf16_f32 v148, v14, v15
	v_cvt_pk_bf16_f32 v149, v16, v17
	v_mfma_f32_32x32x16_bf16 v[66:81], v[154:157], v[202:205], v[66:81]
	s_nop 0
	v_mfma_f32_32x32x16_bf16 v[82:97], v[142:145], v[146:149], v[82:97]
	v_mfma_f32_32x32x16_bf16 v[66:81], v[158:161], v[146:149], v[66:81]
	v_mfma_f32_32x32x16_bf16 v[114:129], v[138:141], v[146:149], v[114:129]
	v_mfma_f32_32x32x16_bf16 v[98:113], v[150:153], v[146:149], v[98:113]
	ds_read_b128 v[138:141], v190 offset:4096
	ds_read_b128 v[142:145], v190 offset:5120
	ds_read_b128 v[146:149], v190 offset:20480
	ds_read_b128 v[150:153], v190 offset:21504
	ds_read_b128 v[154:157], v190 offset:12288
	ds_read_b128 v[158:161], v190 offset:13312
	ds_read_b128 v[202:205], v190 offset:28672
	ds_read_b128 v[206:209], v190 offset:29696
	v_cvt_pk_bf16_f32 v210, v18, v19
	v_cvt_pk_bf16_f32 v211, v20, v21
	v_cvt_pk_bf16_f32 v212, v22, v23
	v_cvt_pk_bf16_f32 v213, v24, v25
	s_waitcnt lgkmcnt(8)
	s_nop 0
	v_mfma_f32_32x32x16_bf16 v[82:97], v[170:173], v[210:213], v[82:97]
	v_mfma_f32_32x32x16_bf16 v[66:81], v[186:189], v[210:213], v[66:81]
	v_mfma_f32_32x32x16_bf16 v[114:129], v[162:165], v[210:213], v[114:129]
	v_cvt_pk_bf16_f32 v162, v26, v27
	v_cvt_pk_bf16_f32 v163, v28, v29
	v_cvt_pk_bf16_f32 v164, v30, v31
	v_cvt_pk_bf16_f32 v165, v32, v33
	v_mfma_f32_32x32x16_bf16 v[98:113], v[178:181], v[210:213], v[98:113]
	s_nop 0
	v_mfma_f32_32x32x16_bf16 v[82:97], v[174:177], v[162:165], v[82:97]
	v_mfma_f32_32x32x16_bf16 v[66:81], v[198:201], v[162:165], v[66:81]
	v_mfma_f32_32x32x16_bf16 v[114:129], v[166:169], v[162:165], v[114:129]
	v_mfma_f32_32x32x16_bf16 v[98:113], v[182:185], v[162:165], v[98:113]
	ds_read_b128 v[162:165], v190 offset:6144
	ds_read_b128 v[166:169], v190 offset:7168
	ds_read_b128 v[170:173], v190 offset:22528
	ds_read_b128 v[174:177], v190 offset:23552
	ds_read_b128 v[178:181], v190 offset:14336
	ds_read_b128 v[182:185], v190 offset:15360
	ds_read_b128 v[186:189], v190 offset:30720
	ds_read_b128 v[198:201], v190 offset:31744
	v_cvt_pk_bf16_f32 v210, v34, v35
	v_cvt_pk_bf16_f32 v211, v36, v37
	v_cvt_pk_bf16_f32 v212, v38, v39
	v_cvt_pk_bf16_f32 v213, v40, v41
	s_waitcnt lgkmcnt(8)
	s_nop 0
	v_mfma_f32_32x32x16_bf16 v[82:97], v[146:149], v[210:213], v[82:97]
	v_mfma_f32_32x32x16_bf16 v[66:81], v[202:205], v[210:213], v[66:81]
	v_mfma_f32_32x32x16_bf16 v[114:129], v[138:141], v[210:213], v[114:129]
	v_cvt_pk_bf16_f32 v138, v42, v43
	v_cvt_pk_bf16_f32 v139, v44, v45
	v_cvt_pk_bf16_f32 v140, v46, v47
	v_cvt_pk_bf16_f32 v141, v48, v49
	v_mfma_f32_32x32x16_bf16 v[98:113], v[154:157], v[210:213], v[98:113]
	s_nop 0
	v_mfma_f32_32x32x16_bf16 v[82:97], v[150:153], v[138:141], v[82:97]
	v_mfma_f32_32x32x16_bf16 v[66:81], v[206:209], v[138:141], v[66:81]
	v_mfma_f32_32x32x16_bf16 v[114:129], v[142:145], v[138:141], v[114:129]
	v_mfma_f32_32x32x16_bf16 v[98:113], v[158:161], v[138:141], v[98:113]
	s_barrier
	ds_read_b128 v[138:141], v191 offset:57344
	ds_read_b128 v[142:145], v191 offset:58368
	ds_read_b128 v[146:149], v191 offset:59392
	ds_read_b128 v[150:153], v191 offset:60416
	ds_read_b128 v[154:157], v191 offset:61440
	ds_read_b128 v[158:161], v191 offset:62464
	ds_read_b128 v[202:205], v191 offset:63488
	ds_read_b128 v[206:209], v191 offset:64512
	v_cvt_pk_bf16_f32 v210, v50, v51
	v_cvt_pk_bf16_f32 v211, v52, v53
	v_cvt_pk_bf16_f32 v212, v54, v55
	v_cvt_pk_bf16_f32 v213, v56, v57
	s_waitcnt lgkmcnt(8)
	s_nop 0
	v_mfma_f32_32x32x16_bf16 v[82:97], v[170:173], v[210:213], v[82:97]
	v_mfma_f32_32x32x16_bf16 v[66:81], v[186:189], v[210:213], v[66:81]
	v_mfma_f32_32x32x16_bf16 v[114:129], v[162:165], v[210:213], v[114:129]
	v_cvt_pk_bf16_f32 v162, v58, v59
	v_cvt_pk_bf16_f32 v163, v60, v61
	v_cvt_pk_bf16_f32 v164, v62, v63
	v_cvt_pk_bf16_f32 v165, v64, v65
	v_mfma_f32_32x32x16_bf16 v[98:113], v[178:181], v[210:213], v[98:113]
	s_nop 0
	v_mfma_f32_32x32x16_bf16 v[82:97], v[174:177], v[162:165], v[82:97]
	v_mfma_f32_32x32x16_bf16 v[66:81], v[198:201], v[162:165], v[66:81]
	v_mfma_f32_32x32x16_bf16 v[114:129], v[166:169], v[162:165], v[114:129]
	v_mfma_f32_32x32x16_bf16 v[98:113], v[182:185], v[162:165], v[98:113]
	ds_read_b128 v[162:165], v190 offset:32768
	ds_read_b128 v[166:169], v190 offset:33792
	ds_read_b128 v[170:173], v190 offset:34816
	ds_read_b128 v[174:177], v190 offset:35840
	ds_read_b128 v[178:181], v190 offset:36864
	ds_read_b128 v[182:185], v190 offset:37888
	ds_read_b128 v[186:189], v190 offset:38912
	ds_read_b128 v[198:201], v190 offset:39936
	s_waitcnt lgkmcnt(8)
	s_nop 1
	v_pk_add_f32 v[114:115], v[138:139], v[114:115] neg_lo:[0,1] neg_hi:[0,1]
	v_pk_add_f32 v[116:117], v[140:141], v[116:117] neg_lo:[0,1] neg_hi:[0,1]
	v_pk_add_f32 v[118:119], v[142:143], v[118:119] neg_lo:[0,1] neg_hi:[0,1]
	v_pk_add_f32 v[122:123], v[146:147], v[122:123] neg_lo:[0,1] neg_hi:[0,1]
	v_pk_add_f32 v[120:121], v[144:145], v[120:121] neg_lo:[0,1] neg_hi:[0,1]
	v_pk_add_f32 v[124:125], v[148:149], v[124:125] neg_lo:[0,1] neg_hi:[0,1]
	v_pk_add_f32 v[126:127], v[150:151], v[126:127] neg_lo:[0,1] neg_hi:[0,1]
	v_cvt_pk_bf16_f32 v114, v114, v115
	v_cvt_pk_bf16_f32 v115, v116, v117
	v_cvt_pk_bf16_f32 v116, v118, v119
	v_cvt_pk_bf16_f32 v118, v122, v123
	v_pk_add_f32 v[122:123], v[152:153], v[128:129] neg_lo:[0,1] neg_hi:[0,1]
	v_pk_add_f32 v[98:99], v[154:155], v[98:99] neg_lo:[0,1] neg_hi:[0,1]
	v_pk_add_f32 v[100:101], v[156:157], v[100:101] neg_lo:[0,1] neg_hi:[0,1]
	v_pk_add_f32 v[102:103], v[158:159], v[102:103] neg_lo:[0,1] neg_hi:[0,1]
	v_pk_add_f32 v[104:105], v[160:161], v[104:105] neg_lo:[0,1] neg_hi:[0,1]
	v_pk_add_f32 v[106:107], v[202:203], v[106:107] neg_lo:[0,1] neg_hi:[0,1]
	v_pk_add_f32 v[108:109], v[204:205], v[108:109] neg_lo:[0,1] neg_hi:[0,1]
	v_pk_add_f32 v[110:111], v[206:207], v[110:111] neg_lo:[0,1] neg_hi:[0,1]
	v_sub_f32_e32 v113, v209, v113
	v_sub_f32_e32 v112, v208, v112
	v_cvt_pk_bf16_f32 v117, v120, v121
	v_cvt_pk_bf16_f32 v119, v124, v125
	v_cvt_pk_bf16_f32 v120, v126, v127
	v_cvt_pk_bf16_f32 v121, v122, v123
	v_cvt_pk_bf16_f32 v98, v98, v99
	v_cvt_pk_bf16_f32 v99, v100, v101
	v_cvt_pk_bf16_f32 v100, v102, v103
	v_cvt_pk_bf16_f32 v101, v104, v105
	v_cvt_pk_bf16_f32 v102, v106, v107
	v_cvt_pk_bf16_f32 v103, v108, v109
	v_cvt_pk_bf16_f32 v104, v110, v111
	v_cvt_pk_bf16_f32 v105, v112, v113
	ds_read_b128 v[106:109], v190 offset:40960
	ds_read_b128 v[110:113], v190 offset:41984
	ds_read_b128 v[122:125], v190 offset:43008
	ds_read_b128 v[126:129], v190 offset:44032
	ds_read_b128 v[138:141], v190 offset:45056
	ds_read_b128 v[142:145], v190 offset:46080
	ds_read_b128 v[146:149], v190 offset:47104
	ds_read_b128 v[150:153], v190 offset:48128
	s_waitcnt lgkmcnt(8)
	v_mfma_f32_32x32x16_bf16 v[82:97], v[162:165], v[114:117], v[82:97]
	v_mfma_f32_32x32x16_bf16 v[66:81], v[178:181], v[114:117], v[66:81]
	v_mfma_f32_32x32x16_bf16 v[82:97], v[166:169], v[118:121], v[82:97]
	v_mfma_f32_32x32x16_bf16 v[66:81], v[182:185], v[118:121], v[66:81]
	v_mfma_f32_32x32x16_bf16 v[82:97], v[170:173], v[98:101], v[82:97]
	v_mfma_f32_32x32x16_bf16 v[66:81], v[186:189], v[98:101], v[66:81]
	v_mfma_f32_32x32x16_bf16 v[82:97], v[174:177], v[102:105], v[82:97]
	v_mfma_f32_32x32x16_bf16 v[66:81], v[198:201], v[102:105], v[66:81]
	ds_read_b128 v[154:157], v190 offset:49152
	ds_read_b128 v[158:161], v190 offset:50176
	ds_read_b128 v[162:165], v190 offset:51200
	ds_read_b128 v[166:169], v190 offset:52224
	ds_read_b128 v[170:173], v190 offset:53248
	ds_read_b128 v[174:177], v190 offset:54272
	ds_read_b128 v[178:181], v190 offset:55296
	ds_read_b128 v[182:185], v190 offset:56320
	v_pk_mul_f32 v[16:17], v[16:17], v[134:135] op_sel_hi:[1,0]
	v_pk_mul_f32 v[14:15], v[14:15], v[134:135] op_sel_hi:[1,0]
	v_pk_mul_f32 v[12:13], v[12:13], v[134:135] op_sel_hi:[1,0]
	v_pk_mul_f32 v[10:11], v[10:11], v[134:135] op_sel_hi:[1,0]
	v_pk_mul_f32 v[8:9], v[8:9], v[134:135] op_sel_hi:[1,0]
	v_pk_mul_f32 v[6:7], v[6:7], v[134:135] op_sel_hi:[1,0]
	v_pk_mul_f32 v[4:5], v[4:5], v[134:135] op_sel_hi:[1,0]
	v_pk_mul_f32 v[2:3], v[2:3], v[134:135] op_sel_hi:[1,0]
	v_pk_mul_f32 v[32:33], v[32:33], v[134:135] op_sel_hi:[1,0]
	v_pk_mul_f32 v[30:31], v[30:31], v[134:135] op_sel_hi:[1,0]
	v_pk_mul_f32 v[28:29], v[28:29], v[134:135] op_sel_hi:[1,0]
	v_pk_mul_f32 v[26:27], v[26:27], v[134:135] op_sel_hi:[1,0]
	v_pk_mul_f32 v[24:25], v[24:25], v[134:135] op_sel_hi:[1,0]
	v_pk_mul_f32 v[22:23], v[22:23], v[134:135] op_sel_hi:[1,0]
	v_pk_mul_f32 v[20:21], v[20:21], v[134:135] op_sel_hi:[1,0]
	v_pk_mul_f32 v[18:19], v[18:19], v[134:135] op_sel_hi:[1,0]
	s_waitcnt lgkmcnt(8)
	v_mfma_f32_32x32x16_bf16 v[2:17], v[106:109], v[114:117], v[2:17]
	v_mfma_f32_32x32x16_bf16 v[18:33], v[138:141], v[114:117], v[18:33]
	v_mfma_f32_32x32x16_bf16 v[2:17], v[110:113], v[118:121], v[2:17]
	v_mfma_f32_32x32x16_bf16 v[18:33], v[142:145], v[118:121], v[18:33]
	v_mfma_f32_32x32x16_bf16 v[2:17], v[122:125], v[98:101], v[2:17]
	v_mfma_f32_32x32x16_bf16 v[18:33], v[146:149], v[98:101], v[18:33]
	v_mfma_f32_32x32x16_bf16 v[2:17], v[126:129], v[102:105], v[2:17]
	v_mfma_f32_32x32x16_bf16 v[18:33], v[150:153], v[102:105], v[18:33]
	v_mul_f32_e64 v48, v48, v134
	v_mul_f32_e64 v49, v49, v134
	v_mul_f32_e64 v46, v46, v134
	v_mul_f32_e64 v47, v47, v134
	v_mul_f32_e64 v44, v44, v134
	v_mul_f32_e64 v45, v45, v134
	v_pk_mul_f32 v[42:43], v[42:43], v[134:135] op_sel_hi:[1,0]
	v_pk_mul_f32 v[40:41], v[40:41], v[134:135] op_sel_hi:[1,0]
	v_pk_mul_f32 v[38:39], v[38:39], v[134:135] op_sel_hi:[1,0]
	v_pk_mul_f32 v[36:37], v[36:37], v[134:135] op_sel_hi:[1,0]
	v_pk_mul_f32 v[34:35], v[34:35], v[134:135] op_sel_hi:[1,0]
	v_pk_mul_f32 v[64:65], v[64:65], v[134:135] op_sel_hi:[1,0]
	v_pk_mul_f32 v[62:63], v[62:63], v[134:135] op_sel_hi:[1,0]
	v_pk_mul_f32 v[60:61], v[60:61], v[134:135] op_sel_hi:[1,0]
	v_pk_mul_f32 v[58:59], v[58:59], v[134:135] op_sel_hi:[1,0]
	v_pk_mul_f32 v[56:57], v[56:57], v[134:135] op_sel_hi:[1,0]
	v_pk_mul_f32 v[54:55], v[54:55], v[134:135] op_sel_hi:[1,0]
	v_pk_mul_f32 v[52:53], v[52:53], v[134:135] op_sel_hi:[1,0]
	v_pk_mul_f32 v[50:51], v[50:51], v[134:135] op_sel_hi:[1,0]
	s_waitcnt lgkmcnt(0)
	v_mfma_f32_32x32x16_bf16 v[34:49], v[154:157], v[114:117], v[34:49]
	s_mov_b64 s[8:9], -1
	s_cmpk_gt_i32 s10, 0xff
	v_mfma_f32_32x32x16_bf16 v[50:65], v[170:173], v[114:117], v[50:65]
	v_mfma_f32_32x32x16_bf16 v[34:49], v[158:161], v[118:121], v[34:49]
	v_mfma_f32_32x32x16_bf16 v[50:65], v[174:177], v[118:121], v[50:65]
	v_mfma_f32_32x32x16_bf16 v[34:49], v[162:165], v[98:101], v[34:49]
	v_mfma_f32_32x32x16_bf16 v[50:65], v[178:181], v[98:101], v[50:65]
	v_mfma_f32_32x32x16_bf16 v[34:49], v[166:169], v[102:105], v[34:49]
	v_mfma_f32_32x32x16_bf16 v[50:65], v[182:185], v[102:105], v[50:65]
	s_cbranch_scc0 .LBB0_771
	s_lshl_b32 s11, s10, 6
	s_mov_b64 s[8:9], 0
